# speedup vs baseline: 1.0147x; 1.0076x over previous
.Lg1_cloop:
	s_lshl_b32 s12, s8, 14
	v_add3_u32 v42, s12, v37, v35
	v_add3_u32 v58, s12, v36, v35
	s_waitcnt vmcnt(3)
	s_barrier
	ds_read_b128 v[38:41], v42 offset:8192
	ds_read_b128 v[42:45], v42 offset:9216
	ds_read_b128 v[46:49], v58
	ds_read_b128 v[50:53], v58 offset:1024
	ds_read_b128 v[54:57], v58 offset:2048
	ds_read_b128 v[58:61], v58 offset:3072
	s_lshl_b32 s13, s17, 14
	s_add_i32 m0, s13, s16
	s_add_i32 s13, s17, 1
	global_load_lds_dwordx4 v62, s[14:15]
	s_cmp_lg_u32 s17, 4
	s_cselect_b32 s17, s13, 0
	v_add_u32_e32 v62, 64, v62
	s_waitcnt lgkmcnt(3)
	v_mfma_f32_16x16x32_f16 v[30:33], v[46:49], v[38:41], v[30:33]
	s_add_i32 s12, s8, 1
	s_cmp_lg_u32 s8, 4
	s_cselect_b32 s8, s12, 0
	v_mfma_f32_16x16x32_f16 v[22:25], v[46:49], v[42:45], v[22:25]
	s_add_i32 s11, s11, -1
	s_cmp_eq_u32 s11, 0
	s_waitcnt lgkmcnt(2)
	v_mfma_f32_16x16x32_f16 v[26:29], v[50:53], v[38:41], v[26:29]
	v_mfma_f32_16x16x32_f16 v[14:17], v[50:53], v[42:45], v[14:17]
	s_waitcnt lgkmcnt(1)
	v_mfma_f32_16x16x32_f16 v[18:21], v[54:57], v[38:41], v[18:21]
	v_mfma_f32_16x16x32_f16 v[6:9], v[54:57], v[42:45], v[6:9]
	s_waitcnt lgkmcnt(0)
	v_mfma_f32_16x16x32_f16 v[10:13], v[58:61], v[38:41], v[10:13]
	v_mfma_f32_16x16x32_f16 v[2:5], v[58:61], v[42:45], v[2:5]
	s_cbranch_scc0 .Lg1_cloop
	s_or_b32 s8, s10, s4
	v_or_b32_e32 v35, s8, v34
	v_lshl_or_b32 v34, v1, 2, s9
	v_mov_b32_e32 v37, 0
	v_or_b32_e32 v34, s7, v34
	v_lshlrev_b32_e32 v36, 12, v35
	v_mov_b32_e32 v35, v37
	v_lshl_add_u64 v[38:39], s[2:3], 0, v[36:37]
	v_lshlrev_b64 v[40:41], 2, v[34:35]
	v_lshl_add_u64 v[42:43], v[38:39], 0, v[40:41]
	s_mov_b64 s[2:3], 0x10000
	v_lshl_add_u64 v[44:45], v[42:43], 0, s[2:3]
	global_store_dwordx4 v[42:43], v[30:33], off sc1
	global_store_dwordx4 v[42:43], v[26:29], off offset:64 sc1
	global_store_dwordx4 v[42:43], v[18:21], off offset:128 sc1
	global_store_dwordx4 v[42:43], v[10:13], off offset:192 sc1
	global_store_dwordx4 v[44:45], v[22:25], off sc1
	global_store_dwordx4 v[44:45], v[14:17], off offset:64 sc1
	global_store_dwordx4 v[44:45], v[6:9], off offset:128 sc1
	global_store_dwordx4 v[44:45], v[2:5], off offset:192 sc1
	s_branch .LBB3_2
